# window phase: dropped the full vmcnt(0) drain before the per-unit q conversion (ring wait already covers the older q loads)
# baseline (speedup 1.0000x reference)
; __device__ __forceinline__ void gs8_init(GS8& g, const bf16* qrow32) {
; #pragma unroll
;     for (int i = 0; i < 4; ++i) { const u32x4 w = *(const GAS u32x4*)(qrow32 + 8 * i);
;         g.q8[2 * i] = (int)pk4_fp8(bf_lo(w.x) * 8.f, bf_hi(w.x) * 8.f, bf_lo(w.y) * 8.f, bf_hi(w.y) * 8.f); g.q8[2 * i + 1] = (int)pk4_fp8(bf_lo(w.z) * 8.f, bf_hi(w.z) * 8.f, bf_lo(w.w) * 8.f, bf_hi(w.w) * 8.f); }
; #pragma unroll
;     for (int dt = 0; dt < 8; ++dt) g.o[dt] = (f32x4){0.f, 0.f, 0.f, 0.f};
;     g.m = -1e30f; g.l = 0.f;
; }
;     i32x8a kf[4];
; #pragma unroll
;     for (int T_ = 0; T_ < 4; ++T_) { kf[T_].lo = *(const LAS i32x4a*)(kl8 + T_ * 16 * K8ST); kf[T_].hi = *(const LAS i32x4a*)(kl8 + T_ * 16 * K8ST + 16); }
;     asm volatile("s_waitcnt lgkmcnt(0)" ::: "memory"); SBAR();
; #pragma unroll
;     for (int T_ = 0; T_ < 4; ++T_) { s0[T_] = __builtin_amdgcn_mfma_scale_f32_16x16x128_f8f6f4(kf[T_], g0.q8, (f32x4){c0, c0, c0, c0}, 0, 0, 0, 0x7f7f7f7f, 0, 0x7c7c7c7c);
;         s1[T_] = __builtin_amdgcn_mfma_scale_f32_16x16x128_f8f6f4(kf[T_], g1.q8, (f32x4){c1, c1, c1, c1}, 0, 0, 0, 0x7f7f7f7f, 0, 0x7c7c7c7c); }
; }
; __device__ __forceinline__ void mask_scores(f32x4 (&s)[4], int a, unsigned W, int kb, int q4) {
;     const float NEG = -__builtin_inff();
; #pragma unroll
;     for (int T_ = 0; T_ < 4; ++T_)
; #pragma unroll
;         for (int i = 0; i < 4; ++i) if ((unsigned)(a - (kb + 16 * T_ + 4 * q4 + i)) >= W) s[T_][i] = NEG;
; }
;     float mx = s[0][0];
; #pragma unroll
;     for (int T_ = 0; T_ < 4; ++T_)
; #pragma unroll
;         for (int i = 0; i < 4; ++i) mx = fmaxf(mx, s[T_][i]);
;     mx += rowbias;
;     float mn = g.m;
;     if (!__all(mx <= g.m + thr)) {
;         mx = xmax32(xmax16(mx));
;         mn = fmaxf(g.m, mx); const float al = __builtin_amdgcn_exp2f(g.m - mn); g.m = mn; g.l *= al;
;         if (WITH_O) {
; #pragma unroll
;             for (int dt = 0; dt < 8; ++dt) g.o[dt] = g.o[dt] * al; }
;     }
;     float ps = 0.f;
; #pragma unroll
;     for (int T_ = 0; T_ < 4; ++T_)
; #pragma unroll
;         for (int i = 0; i < 4; ++i) { s[T_][i] = __builtin_amdgcn_exp2f(s[T_][i] + (rowbias - mn)); ps += s[T_][i]; }
;     g.l += ps;
; }
; template <bool WITH_O, class G> __device__ __forceinline__ void online_smc(f32x4 (&s)[4], G& g, const float ref) {
;     float mx = s[0][0];
; #pragma unroll
;     for (int T_ = 0; T_ < 4; ++T_)
; #pragma unroll
.LBB0_1463:
	v_lshlrev_b32_e32 v16, 16, v0
	v_and_b32_e32 v0, 0xffff0000, v0
	v_mul_f32_e32 v16, 0x41000000, v16
	v_mul_f32_e32 v17, 0x41000000, v0
	v_lshlrev_b32_e32 v18, 16, v1
	v_and_b32_e32 v19, 0xffff0000, v1
	v_mov_b32_e32 v0, v125
	v_lshlrev_b32_e32 v1, 16, v2
	v_cvt_pk_fp8_f32 v0, v16, v17
	v_mul_f32_e32 v16, 0x41000000, v1
	v_and_b32_e32 v1, 0xffff0000, v2
	v_mul_f32_e32 v2, 0x41000000, v1
	v_mov_b32_e32 v1, v125
	v_cvt_pk_fp8_f32 v1, v16, v2
	v_lshlrev_b32_e32 v2, 16, v92
	v_lshlrev_b32_e32 v17, 16, v3
	v_and_b32_e32 v20, 0xffff0000, v3
	v_mul_f32_e32 v3, 0x41000000, v2
	v_and_b32_e32 v2, 0xffff0000, v92
	v_mul_f32_e32 v16, 0x41000000, v2
	v_mov_b32_e32 v2, v125
	v_cvt_pk_fp8_f32 v2, v3, v16
	v_lshlrev_b32_e32 v3, 16, v94
	v_mul_f32_e32 v16, 0x41000000, v3
	v_and_b32_e32 v3, 0xffff0000, v94
	v_mul_f32_e32 v23, 0x41000000, v3
	v_mov_b32_e32 v3, v125
	v_cvt_pk_fp8_f32 v3, v16, v23
	v_lshlrev_b32_e32 v16, 16, v4
	v_and_b32_e32 v4, 0xffff0000, v4
	v_mul_f32_e32 v16, 0x41000000, v16
	v_mul_f32_e32 v23, 0x41000000, v4
	v_lshlrev_b32_e32 v26, 16, v5
	v_and_b32_e32 v27, 0xffff0000, v5
	v_mov_b32_e32 v4, v125
	v_lshlrev_b32_e32 v5, 16, v6
	v_cvt_pk_fp8_f32 v4, v16, v23
	v_mul_f32_e32 v16, 0x41000000, v5
	v_and_b32_e32 v5, 0xffff0000, v6
	v_mul_f32_e32 v6, 0x41000000, v5
	v_mov_b32_e32 v5, v125
	v_cvt_pk_fp8_f32 v5, v16, v6
	v_lshlrev_b32_e32 v6, 16, v88
	v_lshlrev_b32_e32 v23, 16, v7
	v_and_b32_e32 v28, 0xffff0000, v7
	v_mul_f32_e32 v7, 0x41000000, v6
	v_and_b32_e32 v6, 0xffff0000, v88
	v_mul_f32_e32 v16, 0x41000000, v6
	v_mov_b32_e32 v6, v125
	v_cvt_pk_fp8_f32 v6, v7, v16
	v_lshlrev_b32_e32 v7, 16, v90
	v_mul_f32_e32 v16, 0x41000000, v7
	v_and_b32_e32 v7, 0xffff0000, v90
	v_mul_f32_e32 v31, 0x41000000, v7
	v_mov_b32_e32 v7, v125
	v_cvt_pk_fp8_f32 v7, v16, v31
	v_mul_f32_e32 v16, 0x41000000, v18
	v_mul_f32_e32 v18, 0x41000000, v19
	v_lshlrev_b32_e32 v21, 16, v93
	v_and_b32_e32 v22, 0xffff0000, v93
	v_cvt_pk_fp8_f32 v0, v16, v18 op_sel:[0,0,1]
	v_mul_f32_e32 v16, 0x41000000, v17
	v_mul_f32_e32 v17, 0x41000000, v20
	v_lshlrev_b32_e32 v24, 16, v95
	v_and_b32_e32 v25, 0xffff0000, v95
	v_cvt_pk_fp8_f32 v1, v16, v17 op_sel:[0,0,1]
	v_mul_f32_e32 v16, 0x41000000, v21
	v_mul_f32_e32 v17, 0x41000000, v22
	v_cvt_pk_fp8_f32 v2, v16, v17 op_sel:[0,0,1]
	v_mul_f32_e32 v16, 0x41000000, v24
	v_mul_f32_e32 v17, 0x41000000, v25
	v_cvt_pk_fp8_f32 v3, v16, v17 op_sel:[0,0,1]
	v_mul_f32_e32 v16, 0x41000000, v26
	v_mul_f32_e32 v17, 0x41000000, v27
	v_lshlrev_b32_e32 v29, 16, v89
	v_and_b32_e32 v30, 0xffff0000, v89
	v_cvt_pk_fp8_f32 v4, v16, v17 op_sel:[0,0,1]
	v_mul_f32_e32 v16, 0x41000000, v23
	v_mul_f32_e32 v17, 0x41000000, v28
	v_lshlrev_b32_e32 v32, 16, v91
	v_and_b32_e32 v33, 0xffff0000, v91
	v_cvt_pk_fp8_f32 v5, v16, v17 op_sel:[0,0,1]
	v_mul_f32_e32 v16, 0x41000000, v29
	v_mul_f32_e32 v17, 0x41000000, v30
	v_cvt_pk_fp8_f32 v6, v16, v17 op_sel:[0,0,1]
	v_mul_f32_e32 v16, 0x41000000, v32
	v_mul_f32_e32 v17, 0x41000000, v33
	v_cvt_pk_fp8_f32 v7, v16, v17 op_sel:[0,0,1]
	ds_read_b128 v[16:19], v147
	ds_read_b128 v[20:23], v147 offset:16
	ds_read_b128 v[24:27], v147 offset:2304
	ds_read_b128 v[28:31], v147 offset:2320
	ds_read_b128 v[32:35], v147 offset:4608
	ds_read_b128 v[36:39], v147 offset:4624
	ds_read_b128 v[40:43], v147 offset:6912
	ds_read_b128 v[44:47], v147 offset:6928
	s_waitcnt lgkmcnt(0)
	v_add_u32_e32 v64, v96, v114
	s_mov_b32 s6, s4
	s_mov_b32 s7, s4
	s_mov_b32 s5, s4
	v_mov_b64_e32 v[52:53], s[6:7]
	v_mov_b64_e32 v[50:51], s[4:5]
	v_add_u32_e32 v68, 48, v64
	v_add_u32_e32 v67, 49, v64
	s_waitcnt lgkmcnt(0)
	v_mfma_scale_f32_16x16x128_f8f6f4 v[54:57], v[40:47], v[0:7], v[50:53], v149, v148 op_sel_hi:[0,0,0]
	v_sub_u32_e32 v72, s37, v68
	v_add_u32_e32 v66, 50, v64
	v_sub_u32_e32 v49, v124, v67
	v_mov_b32_e32 v48, s46
	v_cmp_gt_u32_e32 vcc, s45, v72
	v_add_u32_e32 v65, 51, v64
	v_sub_u32_e32 v63, v124, v66
	v_mfma_scale_f32_16x16x128_f8f6f4 v[92:95], v[32:39], v[0:7], v[50:53], v149, v148 op_sel_hi:[0,0,0]
	s_nop 3
	v_cndmask_b32_e32 v48, v48, v54, vcc
	v_cmp_gt_u32_e32 vcc, s45, v49
	v_add_u32_e32 v73, 32, v64
	v_sub_u32_e32 v62, v124, v65
	v_cndmask_b32_e32 v49, v150, v55, vcc
	v_cmp_gt_u32_e32 vcc, s45, v63
	v_add_u32_e32 v71, 33, v64
	v_mfma_scale_f32_16x16x128_f8f6f4 v[58:61], v[24:31], v[0:7], v[50:53], v149, v148 op_sel_hi:[0,0,0]
	v_sub_u32_e32 v54, s37, v73
	v_add_u32_e32 v70, 34, v64
	v_sub_u32_e32 v55, v124, v71
	v_add_u32_e32 v69, 35, v64
	v_add_u32_e32 v77, 16, v64
	v_add_u32_e32 v76, 17, v64
	v_sub_u32_e32 v72, s37, v77
	v_mfma_scale_f32_16x16x128_f8f6f4 v[88:91], v[16:23], v[0:7], v[50:53], v149, v148 op_sel_hi:[0,0,0]
	v_add_u32_e32 v75, 18, v64
	v_sub_u32_e32 v63, v124, v76
	v_add_u32_e32 v74, 19, v64
	v_or_b32_e32 v79, 2, v64
	v_or_b32_e32 v78, 3, v64
	s_nop 1
	v_cndmask_b32_e32 v50, v150, v56, vcc
	v_cmp_gt_u32_e32 vcc, s45, v62
	v_mov_b32_e32 v52, s46
	v_sub_u32_e32 v56, v124, v70
	v_cndmask_b32_e32 v51, v150, v57, vcc
	v_cmp_gt_u32_e32 vcc, s45, v54
	v_sub_u32_e32 v53, v124, v69
	v_sub_u32_e32 v62, v124, v75
	v_cndmask_b32_e32 v54, v52, v92, vcc
	v_cmp_gt_u32_e32 vcc, s45, v55
	v_sub_u32_e32 v57, v124, v74
	v_mov_b32_e32 v135, 0xf149f2ca
	v_cndmask_b32_e32 v55, v150, v93, vcc
	v_cmp_gt_u32_e32 vcc, s45, v56
	v_mov_b32_e32 v56, s46
	s_nop 0
	v_cndmask_b32_e32 v52, v150, v94, vcc
	v_cmp_gt_u32_e32 vcc, s45, v53
	s_nop 1
	v_cndmask_b32_e32 v53, v150, v95, vcc
	v_cmp_gt_u32_e32 vcc, s45, v72
	v_sub_u32_e32 v72, v124, v79
	s_nop 0
	v_cndmask_b32_e32 v58, v56, v58, vcc
	v_cmp_gt_u32_e32 vcc, s45, v63
	v_sub_u32_e32 v63, v64, v124
	s_nop 0
	v_cndmask_b32_e32 v59, v150, v59, vcc
	v_cmp_gt_u32_e32 vcc, s45, v62
	v_sub_u32_e32 v62, s37, v64
	s_nop 0
	v_cndmask_b32_e32 v56, v150, v60, vcc
	v_cmp_gt_u32_e32 vcc, s45, v57
	v_mov_b32_e32 v60, s46
	s_nop 0
	v_cndmask_b32_e32 v57, v150, v61, vcc
	v_cmp_gt_u32_e32 vcc, s45, v62
	v_sub_u32_e32 v61, v124, v78
	s_nop 0
	v_cndmask_b32_e32 v62, v60, v88, vcc
	v_cmp_lt_u32_e32 vcc, s47, v63
	s_nop 1
	v_cndmask_b32_e32 v63, v150, v89, vcc
	v_cmp_gt_u32_e32 vcc, s45, v72
	v_max_f32_e32 v72, v62, v62
	v_max_f32_e32 v88, v63, v63
	v_cndmask_b32_e32 v60, v150, v90, vcc
	v_cmp_gt_u32_e32 vcc, s45, v61
	v_max_f32_e32 v72, v72, v88
	v_mov_b32_e32 v88, 0
	v_cndmask_b32_e32 v61, v150, v91, vcc
	v_max3_f32 v72, v72, v60, v61
	v_max3_f32 v72, v72, v58, v59
	v_max3_f32 v72, v72, v56, v57
	v_max3_f32 v72, v72, v54, v55
	v_max3_f32 v72, v72, v52, v53
	v_max3_f32 v72, v72, v48, v49
	v_max3_f32 v72, v72, v50, v51
	v_cmp_le_f32_e32 vcc, v72, v135
	s_cmp_eq_u64 vcc, exec
	s_cbranch_scc1 .LBB0_1465
; __device__ __forceinline__ float xmax16(float v) { float a = v, b = v; PL_SWAP16(a, b); return fmaxf(a, b); }
; __device__ __forceinline__ float xmax32(float v) { float a = v, b = v; PL_SWAP32(a, b); return fmaxf(a, b); }
; template <bool WITH_O, class G> __device__ __forceinline__ void online_smc(f32x4 (&s)[4], G& g, const float ref) {
;     ...
;     if (!__all(t <= g.m + SM_THR)) {
;         const float mr = xmax32(xmax16(t));
;         const float mn = fmaxf(g.m, mr); const float al = __builtin_amdgcn_exp2f(g.m - mn); g.m = mn; g.l *= al;
;         if (WITH_O) {
; #pragma unroll
;             for (int dt = 0; dt < 8; ++dt) g.o[dt] = g.o[dt] * al; }
;         const float d = ref - mn;
; #pragma unroll
;         for (int T_ = 0; T_ < 4; ++T_)
; #pragma unroll
;             for (int i = 0; i < 4; ++i) s[T_][i] += d;
;     }
	v_add_f32_e32 v72, 0, v72
	v_mov_b32_e32 v89, v72
	s_nop 1
	v_permlane16_swap_b32 v72, v89
	s_nop 0
	v_max_f32_e32 v89, v89, v89
	v_max_f32_e32 v72, v72, v72
	v_max_f32_e32 v72, v72, v89
	v_mov_b32_e32 v89, v72
	s_nop 1
	v_permlane32_swap_b32 v72, v89
	s_nop 0
	v_max3_f32 v137, v72, v89, s48
	v_sub_f32_e32 v72, 0xf149f2ca, v137
	v_exp_f32_e32 v72, v72
	v_sub_f32_e32 v90, 0, v137
	v_pk_add_f32 v[62:63], v[62:63], v[90:91] op_sel_hi:[1,0]
	v_pk_add_f32 v[60:61], v[60:61], v[90:91] op_sel_hi:[1,0]
	v_mul_f32_e32 v72, 0, v72
	v_pk_add_f32 v[58:59], v[58:59], v[90:91] op_sel_hi:[1,0]
	v_pk_add_f32 v[56:57], v[56:57], v[90:91] op_sel_hi:[1,0]
	v_pk_add_f32 v[54:55], v[54:55], v[90:91] op_sel_hi:[1,0]
	v_pk_add_f32 v[52:53], v[52:53], v[90:91] op_sel_hi:[1,0]
	v_pk_add_f32 v[48:49], v[48:49], v[90:91] op_sel_hi:[1,0]
	v_pk_add_f32 v[50:51], v[50:51], v[90:91] op_sel_hi:[1,0]
	s_branch .LBB0_1466
